# adds P2 decay-constant load hoist and the P4 retention/SSD load de-serialisation set (rescale tail loads up front, cross/inner fragment read pipelining, state load)
# speedup vs baseline: 1.0068x; 1.0017x over previous
; #define LAS __attribute__((address_space(3)))
; #define PROJ_AT(X, row, col) (XP_PROJ(X) + (size_t)((col) >> 8) * PANP + (size_t)(row) * 256 + ((col) & 255))
; __device__ __forceinline__ void p2_ret(Ctx& X, int unit) {
;     const int c = unit >> 2, h = unit & 3, t0 = c * CH, tid = X.tid, lane = X.lane, w = X.wave;
;     LAS uchar* Vt = X.lds; LAS uchar* Kt = X.lds + 69632;
;     { u32x4 vv[8], kk[8];
; #pragma unroll
;       for (int i = 0; i < 8; ++i) { const int q = tid + 512 * i, l = q >> 5, vc = q & 31; const bf16* rp = PROJ_AT(X, t0 + l, h * 256 + vc * 8);
;           vv[i] = *(const u32x4*)(rp + (size_t)(C_V >> 8) * PANP); kk[i] = *(const u32x4*)(rp + (size_t)(C_K >> 8) * PANP); }
; #pragma unroll
;       for (int i = 0; i < 8; ++i) { const int q = tid + 512 * i, l = q >> 5, vc = q & 31; *(LAS u32x4*)(Vt + l * 544 + vc * 16) = vv[i]; *(LAS u32x4*)(Kt + l * 544 + vc * 16) = kk[i]; } }
;     __syncthreads();
;     const float lg = LG2_GAMMA[h];
;     float rr[8];
; #pragma unroll
;     for (int e = 0; e < 8; ++e) rr[e] = exp2f(-lg * (float)e);
.LBB0_198:
	s_lshl_b32 s8, s4, 5
	s_and_b32 s9, s8, 0xffffff80
	s_and_b32 s5, s4, 3
	v_or_b32_e32 v2, s9, v143
	s_lshl_b32 s2, s5, 22
	v_ashrrev_i32_e32 v3, 31, v2
	s_waitcnt vmcnt(1)
	v_lshl_add_u64 v[58:59], v[134:135], 0, s[2:3]
	v_lshlrev_b64 v[2:3], 9, v[2:3]
	v_lshl_add_u64 v[2:3], v[58:59], 0, v[2:3]
	v_add_co_u32_e32 v10, vcc, 0x2000000, v2
	s_lshl_b32 s2, s5, 2
	s_nop 0
	v_addc_co_u32_e32 v11, vcc, 0, v3, vcc
	v_add_co_u32_e32 v12, vcc, 0x1000000, v2
	v_mov_b32_e32 v182, v152
	s_nop 0
	v_addc_co_u32_e32 v13, vcc, 0, v3, vcc
	global_load_dwordx4 v[2:5], v[10:11], off
	global_load_dwordx4 v[6:9], v[12:13], off
	v_or_b32_e32 v10, s9, v145
	v_ashrrev_i32_e32 v11, 31, v10
	v_lshlrev_b64 v[10:11], 9, v[10:11]
	v_lshl_add_u64 v[10:11], v[58:59], 0, v[10:11]
	v_add_co_u32_e32 v18, vcc, s6, v10
	v_mov_b32_e32 v70, 0
	s_nop 0
	v_addc_co_u32_e32 v19, vcc, 0, v11, vcc
	v_add_co_u32_e32 v20, vcc, 0x1000000, v10
	v_mov_b32_e32 v71, v133
	s_nop 0
	v_addc_co_u32_e32 v21, vcc, 0, v11, vcc
	global_load_dwordx4 v[10:13], v[18:19], off
	global_load_dwordx4 v[14:17], v[20:21], off
	v_or_b32_e32 v18, s9, v146
	v_ashrrev_i32_e32 v19, 31, v18
	v_lshlrev_b64 v[18:19], 9, v[18:19]
	v_lshl_add_u64 v[18:19], v[58:59], 0, v[18:19]
	v_add_co_u32_e32 v26, vcc, s6, v18
	v_mov_b32_e32 v72, v133
	s_nop 0
	v_addc_co_u32_e32 v27, vcc, 0, v19, vcc
	v_add_co_u32_e32 v28, vcc, 0x1000000, v18
	v_mov_b32_e32 v73, v133
	s_nop 0
	v_addc_co_u32_e32 v29, vcc, 0, v19, vcc
	global_load_dwordx4 v[18:21], v[26:27], off
	global_load_dwordx4 v[22:25], v[28:29], off
	v_or_b32_e32 v26, s9, v147
	v_ashrrev_i32_e32 v27, 31, v26
	v_lshlrev_b64 v[26:27], 9, v[26:27]
	v_lshl_add_u64 v[26:27], v[58:59], 0, v[26:27]
	v_add_co_u32_e32 v34, vcc, s6, v26
	v_mov_b32_e32 v74, 0
	s_nop 0
	v_addc_co_u32_e32 v35, vcc, 0, v27, vcc
	v_add_co_u32_e32 v36, vcc, 0x1000000, v26
	v_mov_b32_e32 v75, v133
	s_nop 0
	v_addc_co_u32_e32 v37, vcc, 0, v27, vcc
	global_load_dwordx4 v[26:29], v[34:35], off
	global_load_dwordx4 v[30:33], v[36:37], off
	v_or_b32_e32 v34, s9, v148
	v_ashrrev_i32_e32 v35, 31, v34
	v_lshlrev_b64 v[34:35], 9, v[34:35]
	v_lshl_add_u64 v[34:35], v[58:59], 0, v[34:35]
	v_add_co_u32_e32 v42, vcc, s6, v34
	s_waitcnt vmcnt(8)
	v_mov_b32_e32 v76, v133
	v_addc_co_u32_e32 v43, vcc, 0, v35, vcc
	v_add_co_u32_e32 v44, vcc, 0x1000000, v34
	v_mov_b32_e32 v77, v133
	s_nop 0
	v_addc_co_u32_e32 v45, vcc, 0, v35, vcc
	global_load_dwordx4 v[34:37], v[42:43], off
	global_load_dwordx4 v[38:41], v[44:45], off
	v_or_b32_e32 v42, s9, v149
	v_ashrrev_i32_e32 v43, 31, v42
	v_lshlrev_b64 v[42:43], 9, v[42:43]
	v_lshl_add_u64 v[42:43], v[58:59], 0, v[42:43]
	v_add_co_u32_e32 v50, vcc, s6, v42
	v_mov_b32_e32 v78, 0
	s_nop 0
	v_addc_co_u32_e32 v51, vcc, 0, v43, vcc
	v_add_co_u32_e32 v52, vcc, 0x1000000, v42
	v_mov_b32_e32 v79, v133
	s_nop 0
	v_addc_co_u32_e32 v53, vcc, 0, v43, vcc
	global_load_dwordx4 v[42:45], v[50:51], off
	global_load_dwordx4 v[46:49], v[52:53], off
	v_or_b32_e32 v50, s8, v150
	v_ashrrev_i32_e32 v51, 31, v50
	v_lshlrev_b64 v[50:51], 9, v[50:51]
	v_lshl_add_u64 v[50:51], v[58:59], 0, v[50:51]
	v_add_co_u32_e32 v60, vcc, s6, v50
	v_mov_b32_e32 v80, v133
	s_nop 0
	v_addc_co_u32_e32 v61, vcc, 0, v51, vcc
	v_add_co_u32_e32 v62, vcc, 0x1000000, v50
	v_mov_b32_e32 v81, v133
	s_nop 0
	v_addc_co_u32_e32 v63, vcc, 0, v51, vcc
	global_load_dwordx4 v[50:53], v[60:61], off
	global_load_dwordx4 v[54:57], v[62:63], off
	v_or_b32_e32 v60, s9, v151
	v_ashrrev_i32_e32 v61, 31, v60
	v_lshlrev_b64 v[60:61], 9, v[60:61]
	v_lshl_add_u64 v[58:59], v[58:59], 0, v[60:61]
	v_add_co_u32_e32 v66, vcc, s6, v58
	s_getpc_b64 s[8:9]
	s_add_u32 s8, s8, LG2_GAMMA@rel32@lo+4
	s_addc_u32 s9, s9, LG2_GAMMA@rel32@hi+12
	s_nop 0
	s_load_dword s2, s[8:9], s2 offset:0x0
	v_addc_co_u32_e32 v67, vcc, 0, v59, vcc
	v_add_co_u32_e32 v68, vcc, 0x1000000, v58
	v_mov_b32_e32 v82, 0
	s_nop 0
	v_addc_co_u32_e32 v69, vcc, 0, v59, vcc
	global_load_dwordx4 v[58:61], v[66:67], off
	global_load_dwordx4 v[62:65], v[68:69], off
	v_mov_b32_e32 v66, 0
	v_mov_b32_e32 v67, v133
	v_mov_b32_e32 v68, v133
	v_mov_b32_e32 v69, v133
	v_mov_b32_e32 v83, v133
	v_mov_b32_e32 v84, v133
	v_mov_b32_e32 v85, v133
	v_mov_b32_e32 v86, 0
	v_mov_b32_e32 v87, v133
	v_mov_b32_e32 v88, v133
	v_mov_b32_e32 v89, v133
	v_mov_b32_e32 v90, 0
	v_mov_b32_e32 v91, v133
	s_waitcnt vmcnt(15)
	ds_write_b128 v155, v[2:5]
	s_waitcnt vmcnt(14)
	ds_write_b128 v156, v[6:9]
	s_waitcnt vmcnt(13)
	ds_write_b128 v157, v[10:13]
	s_waitcnt vmcnt(12)
	ds_write_b128 v159, v[14:17]
	s_waitcnt vmcnt(11)
	ds_write_b128 v155, v[18:21] offset:17408
	s_waitcnt vmcnt(10)
	ds_write_b128 v156, v[22:25] offset:17408
	s_waitcnt vmcnt(9)
	ds_write_b128 v160, v[26:29]
	s_waitcnt vmcnt(8)
	ds_write_b128 v161, v[30:33]
	s_waitcnt vmcnt(7)
	ds_write_b128 v155, v[34:37] offset:34816
	s_waitcnt vmcnt(6)
	ds_write_b128 v156, v[38:41] offset:34816
	s_waitcnt vmcnt(5)
	ds_write_b128 v162, v[42:45]
	s_waitcnt vmcnt(4)
	ds_write_b128 v163, v[46:49]
	s_waitcnt vmcnt(3)
	ds_write_b128 v155, v[50:53] offset:52224
	s_waitcnt vmcnt(2)
	ds_write_b128 v156, v[54:57] offset:52224
	s_waitcnt vmcnt(1)
	ds_write_b128 v164, v[58:61]
	s_waitcnt vmcnt(0)
	ds_write_b128 v165, v[62:65]
	s_waitcnt lgkmcnt(0)
	s_barrier
; __device__ __forceinline__ void p2_ret(Ctx& X, int unit) {
;     ...
;     const float lg = LG2_GAMMA[h];
;     float rr[8];
; #pragma unroll
;     for (int e = 0; e < 8; ++e) rr[e] = exp2f(-lg * (float)e);
;     const int fr = lane & 15, fq = lane >> 4, trs = (8 * fq + ((lane & 15) >> 2)) * 544 + 8 * (lane & 3);
;     f32x4 acc[2][16];
; #pragma unroll
;     for (int a = 0; a < 2; ++a)
; #pragma unroll
;         for (int n = 0; n < 16; ++n) acc[a][n] = (f32x4){0.f, 0.f, 0.f, 0.f};
	v_mov_b32_e32 v4, v133
	v_mov_b32_e32 v5, v133
	v_mov_b32_e32 v6, 0
	v_mov_b32_e32 v7, v133
	s_waitcnt lgkmcnt(0)
	v_mul_f32_e32 v2, s2, v166
	v_cmp_gt_f32_e32 vcc, s7, v2
	s_and_b64 s[8:9], vcc, exec
	s_cselect_b32 s5, 0xffffffc0, 0
	v_cndmask_b32_e32 v2, 0, v167, vcc
	v_cmp_gt_f32_e32 vcc, s2, v168
	v_fmac_f32_e32 v2, s2, v166
	v_exp_f32_e32 v2, v2
	v_cndmask_b32_e32 v3, 0, v167, vcc
	v_subrev_f32_e32 v3, s2, v3
	v_exp_f32_e32 v3, v3
	s_and_b64 s[8:9], vcc, exec
	v_ldexp_f32 v174, v2, s5
	s_cselect_b32 s5, 0xffffffc0, 0
	v_mul_f32_e64 v2, s2, -2.0
	v_ldexp_f32 v175, v3, s5
	v_cmp_gt_f32_e32 vcc, s7, v2
	v_mul_f32_e32 v3, s2, v169
	s_and_b64 s[8:9], vcc, exec
	v_cndmask_b32_e32 v2, 0, v167, vcc
	v_cmp_gt_f32_e32 vcc, s7, v3
	v_fmac_f32_e64 v2, s2, -2.0
	v_exp_f32_e32 v2, v2
	v_cndmask_b32_e32 v3, 0, v167, vcc
	v_fmac_f32_e32 v3, s2, v169
	v_exp_f32_e32 v3, v3
	s_cselect_b32 s5, 0xffffffc0, 0
	s_and_b64 s[8:9], vcc, exec
	v_ldexp_f32 v176, v2, s5
	s_cselect_b32 s5, 0xffffffc0, 0
	v_mul_f32_e64 v2, s2, -4.0
	v_ldexp_f32 v177, v3, s5
	v_cmp_gt_f32_e32 vcc, s7, v2
	v_mul_f32_e32 v3, s2, v170
	s_and_b64 s[8:9], vcc, exec
	v_cndmask_b32_e32 v2, 0, v167, vcc
	v_cmp_gt_f32_e32 vcc, s7, v3
	v_fmac_f32_e64 v2, s2, -4.0
	v_exp_f32_e32 v2, v2
	v_cndmask_b32_e32 v3, 0, v167, vcc
	v_fmac_f32_e32 v3, s2, v170
	v_exp_f32_e32 v3, v3
	s_cselect_b32 s5, 0xffffffc0, 0
	s_and_b64 s[8:9], vcc, exec
	v_ldexp_f32 v178, v2, s5
	s_cselect_b32 s5, 0xffffffc0, 0
	v_mul_f32_e32 v2, s2, v171
	v_ldexp_f32 v179, v3, s5
	v_cmp_gt_f32_e32 vcc, s7, v2
	v_mul_f32_e32 v3, s2, v172
	s_and_b64 s[8:9], vcc, exec
	v_cndmask_b32_e32 v2, 0, v167, vcc
	v_cmp_gt_f32_e32 vcc, s7, v3
	v_fmac_f32_e32 v2, s2, v171
	v_exp_f32_e32 v2, v2
	v_cndmask_b32_e32 v3, 0, v167, vcc
	v_fmac_f32_e32 v3, s2, v172
	v_exp_f32_e32 v3, v3
	s_cselect_b32 s5, 0xffffffc0, 0
	s_and_b64 s[8:9], vcc, exec
	v_ldexp_f32 v180, v2, s5
	s_cselect_b32 s5, 0xffffffc0, 0
	v_ldexp_f32 v181, v3, s5
	s_mov_b32 s5, 0
	v_mov_b32_e32 v2, 0
	v_mov_b32_e32 v3, v133
	v_mov_b32_e32 v8, v133
	v_mov_b32_e32 v9, v133
	v_mov_b32_e32 v10, 0
	v_mov_b32_e32 v11, v133
	v_mov_b32_e32 v12, v133
	v_mov_b32_e32 v13, v133
	v_mov_b32_e32 v14, 0
	v_mov_b32_e32 v15, v133
	v_mov_b32_e32 v16, v133
	v_mov_b32_e32 v17, v133
	v_mov_b32_e32 v18, 0
	v_mov_b32_e32 v19, v133
	v_mov_b32_e32 v20, v133
	v_mov_b32_e32 v21, v133
	v_mov_b32_e32 v22, 0
	v_mov_b32_e32 v23, v133
	v_mov_b32_e32 v24, v133
	v_mov_b32_e32 v25, v133
	v_mov_b32_e32 v26, 0
	v_mov_b32_e32 v27, v133
	v_mov_b32_e32 v28, v133
	v_mov_b32_e32 v29, v133
	v_mov_b32_e32 v30, 0
	v_mov_b32_e32 v31, v133
	v_mov_b32_e32 v32, v133
	v_mov_b32_e32 v33, v133
	v_mov_b32_e32 v34, 0
	v_mov_b32_e32 v35, v133
	v_mov_b32_e32 v36, v133
	v_mov_b32_e32 v37, v133
	v_mov_b32_e32 v38, 0
	v_mov_b32_e32 v39, v133
	v_mov_b32_e32 v40, v133
	v_mov_b32_e32 v41, v133
	v_mov_b32_e32 v42, 0
	v_mov_b32_e32 v43, v133
	v_mov_b32_e32 v44, v133
	v_mov_b32_e32 v45, v133
	v_mov_b32_e32 v46, 0
	v_mov_b32_e32 v47, v133
	v_mov_b32_e32 v48, v133
	v_mov_b32_e32 v49, v133
	v_mov_b32_e32 v50, 0
	v_mov_b32_e32 v51, v133
	v_mov_b32_e32 v52, v133
	v_mov_b32_e32 v53, v133
	v_mov_b32_e32 v54, 0
	v_mov_b32_e32 v55, v133
	v_mov_b32_e32 v56, v133
	v_mov_b32_e32 v57, v133
	v_mov_b32_e32 v58, 0
	v_mov_b32_e32 v59, v133
	v_mov_b32_e32 v60, v133
	v_mov_b32_e32 v61, v133
	v_mov_b32_e32 v62, 0
	v_mov_b32_e32 v63, v133
	v_mov_b32_e32 v64, v133
	v_mov_b32_e32 v65, v133
	v_mov_b32_e32 v92, v133
	v_mov_b32_e32 v93, v133
	v_mov_b32_e32 v94, 0
	v_mov_b32_e32 v95, v133
	v_mov_b32_e32 v96, v133
	v_mov_b32_e32 v97, v133
	v_mov_b32_e32 v98, 0
	v_mov_b32_e32 v99, v133
	v_mov_b32_e32 v100, v133
	v_mov_b32_e32 v101, v133
	v_mov_b32_e32 v102, 0
	v_mov_b32_e32 v103, v133
	v_mov_b32_e32 v104, v133
	v_mov_b32_e32 v105, v133
	v_mov_b32_e32 v106, 0
	v_mov_b32_e32 v107, v133
	v_mov_b32_e32 v108, v133
	v_mov_b32_e32 v109, v133
	v_mov_b32_e32 v110, 0
	v_mov_b32_e32 v111, v133
	v_mov_b32_e32 v112, v133
	v_mov_b32_e32 v113, v133
	v_mov_b32_e32 v114, 0
	v_mov_b32_e32 v115, v133
	v_mov_b32_e32 v116, v133
	v_mov_b32_e32 v117, v133
	v_mov_b32_e32 v118, 0
	v_mov_b32_e32 v119, v133
	v_mov_b32_e32 v120, v133
	v_mov_b32_e32 v121, v133
	v_mov_b32_e32 v122, 0
	v_mov_b32_e32 v123, v133
	v_mov_b32_e32 v124, v133
	v_mov_b32_e32 v125, v133
	v_mov_b32_e32 v126, 0
	v_mov_b32_e32 v127, v133
	v_mov_b32_e32 v128, v133
	v_mov_b32_e32 v129, v133

; __device__ __forceinline__ unsigned pk_bf16(float lo, float hi) { unsigned r; asm("v_cvt_pk_bf16_f32 %0, %1, %2" : "=v"(r) : "v"(lo), "v"(hi)); return r; }
; __device__ __forceinline__ float bf_lo(unsigned u) { return __uint_as_float(u << 16); }
; __device__ __forceinline__ float bf_hi(unsigned u) { return __uint_as_float(u & 0xffff0000u); }
; __device__ __forceinline__ void p4_ssd(Ctx& X, int unit) {
;     ...
;     ss += __shfl_xor(ss, 16); ss += __shfl_xor(ss, 32);
;     const float rstd = rsqrtf(ss * (1.f / 512.f) + EPS);
;     const float* nw = XP_ssm_norm_w(X) + 512 * g + 4 * fq;
;     u32x2 tv[32];
; #pragma unroll
;     for (int i = 0; i < 32; ++i) tv[i] = *(const u32x2*)(op + (size_t)(i >> 2) * PANE_A + 16 * (i & 3));
; #pragma unroll
;     for (int i = 0; i < 32; ++i) { const f32x4 wv = *(const f32x4*)(nw + 16 * i); const u32x2 t = tv[i];
;         u32x2 o; o.x = pk_bf16(bf_lo(t.x) * rstd * wv.x, bf_hi(t.x) * rstd * wv.y); o.y = pk_bf16(bf_lo(t.y) * rstd * wv.z, bf_hi(t.y) * rstd * wv.w);
;         *(u32x2*)(op + (size_t)(i >> 2) * PANE_A + 16 * (i & 3)) = o; }
.LBB0_576:
	s_load_dwordx2 s[6:7], s[0:1], 0x48
	s_load_dwordx4 s[88:91], s[0:1], 0x98
	s_lshl_b32 s4, s13, 2
	v_lshlrev_b32_e32 v87, 2, v98
	global_load_dwordx2 v[2:3], v[118:119], off
	global_load_dwordx2 v[4:5], v[118:119], off offset:32
	global_load_dwordx2 v[6:7], v[118:119], off offset:64
	global_load_dwordx2 v[8:9], v[118:119], off offset:96
	v_add_co_u32_e32 v66, vcc, 0x100000, v118
	s_nop 1
	v_addc_co_u32_e32 v67, vcc, 0, v119, vcc
	global_load_dwordx2 v[10:11], v[66:67], off
	global_load_dwordx2 v[12:13], v[66:67], off offset:32
	global_load_dwordx2 v[14:15], v[66:67], off offset:64
	global_load_dwordx2 v[16:17], v[66:67], off offset:96
	v_add_co_u32_e32 v68, vcc, 0x200000, v118
	s_nop 1
	v_addc_co_u32_e32 v69, vcc, 0, v119, vcc
	global_load_dwordx2 v[18:19], v[68:69], off
	global_load_dwordx2 v[20:21], v[68:69], off offset:32
	global_load_dwordx2 v[22:23], v[68:69], off offset:64
	global_load_dwordx2 v[24:25], v[68:69], off offset:96
	v_add_co_u32_e32 v70, vcc, 0x300000, v118
	s_nop 1
	v_addc_co_u32_e32 v71, vcc, 0, v119, vcc
	global_load_dwordx2 v[26:27], v[70:71], off
	global_load_dwordx2 v[28:29], v[70:71], off offset:32
	global_load_dwordx2 v[30:31], v[70:71], off offset:64
	global_load_dwordx2 v[32:33], v[70:71], off offset:96
	v_add_co_u32_e32 v72, vcc, 0x400000, v118
	s_nop 1
	v_addc_co_u32_e32 v73, vcc, 0, v119, vcc
	global_load_dwordx2 v[34:35], v[72:73], off
	global_load_dwordx2 v[36:37], v[72:73], off offset:32
	global_load_dwordx2 v[38:39], v[72:73], off offset:64
	global_load_dwordx2 v[40:41], v[72:73], off offset:96
	v_add_co_u32_e32 v74, vcc, 0x500000, v118
	s_nop 1
	v_addc_co_u32_e32 v75, vcc, 0, v119, vcc
	global_load_dwordx2 v[42:43], v[74:75], off
	global_load_dwordx2 v[44:45], v[74:75], off offset:32
	global_load_dwordx2 v[46:47], v[74:75], off offset:64
	global_load_dwordx2 v[48:49], v[74:75], off offset:96
	v_add_co_u32_e32 v76, vcc, 0x600000, v118
	s_nop 1
	v_addc_co_u32_e32 v77, vcc, 0, v119, vcc
	global_load_dwordx2 v[50:51], v[76:77], off
	global_load_dwordx2 v[52:53], v[76:77], off offset:32
	global_load_dwordx2 v[54:55], v[76:77], off offset:64
	global_load_dwordx2 v[56:57], v[76:77], off offset:96
	v_add_co_u32_e32 v78, vcc, 0x700000, v118
	s_nop 1
	v_addc_co_u32_e32 v79, vcc, 0, v119, vcc
	global_load_dwordx2 v[58:59], v[78:79], off
	global_load_dwordx2 v[60:61], v[78:79], off offset:32
	global_load_dwordx2 v[62:63], v[78:79], off offset:64
	global_load_dwordx2 v[64:65], v[78:79], off offset:96
	s_waitcnt lgkmcnt(0)
	s_add_u32 s6, s6, s4
	s_addc_u32 s7, s7, 0
	global_load_dwordx4 v[120:123], v87, s[6:7]
	global_load_dwordx4 v[124:127], v87, s[6:7] offset:64
	global_load_dwordx4 v[128:131], v87, s[6:7] offset:128
	global_load_dwordx4 v[132:135], v87, s[6:7] offset:192
	global_load_dwordx4 v[136:139], v87, s[6:7] offset:256
	global_load_dwordx4 v[140:143], v87, s[6:7] offset:320
	global_load_dwordx4 v[144:147], v87, s[6:7] offset:384
	global_load_dwordx4 v[148:151], v87, s[6:7] offset:448
	global_load_dwordx4 v[152:155], v87, s[6:7] offset:512
	global_load_dwordx4 v[224:227], v87, s[6:7] offset:576
	global_load_dwordx4 v[228:231], v87, s[6:7] offset:640
	global_load_dwordx4 v[232:235], v87, s[6:7] offset:704
	global_load_dwordx4 v[236:239], v87, s[6:7] offset:768
	global_load_dwordx4 v[240:243], v87, s[6:7] offset:832
	global_load_dwordx4 v[244:247], v87, s[6:7] offset:896
	global_load_dwordx4 v[214:217], v87, s[6:7] offset:960
	ds_bpermute_b32 v85, v182, v115
	s_mov_b32 s4, 0x800000
	v_readlane_b32 s93, v248, 4
	s_waitcnt lgkmcnt(0)
	v_add_f32_e32 v85, v115, v85
	ds_bpermute_b32 v86, v183, v85
	s_waitcnt lgkmcnt(0)
	v_add_f32_e32 v85, v85, v86
	v_fmamk_f32 v85, v85, 0x3b000000, v197
	v_mul_f32_e32 v86, 0x4b800000, v85
	v_cmp_gt_f32_e32 vcc, s4, v85
	s_nop 1
	v_cndmask_b32_e32 v85, v85, v86, vcc
	v_rsq_f32_e32 v85, v85
	s_nop 0
	v_mul_f32_e32 v86, 0x45800000, v85
	v_cndmask_b32_e32 v80, v85, v86, vcc
	s_waitcnt vmcnt(15)
	v_lshlrev_b32_e32 v81, 16, v2
	v_and_b32_e32 v82, 0xffff0000, v2
	v_lshlrev_b32_e32 v83, 16, v3
	v_and_b32_e32 v84, 0xffff0000, v3
	v_mul_f32_e32 v81, v80, v81
	v_mul_f32_e32 v82, v80, v82
	v_mul_f32_e32 v83, v80, v83
	v_mul_f32_e32 v84, v80, v84
	v_mul_f32_e32 v81, v81, v120
	v_mul_f32_e32 v82, v82, v121
	v_mul_f32_e32 v83, v83, v122
	v_mul_f32_e32 v84, v84, v123
	v_cvt_pk_bf16_f32 v88, v81, v82
	v_cvt_pk_bf16_f32 v89, v83, v84
	global_store_dwordx2 v[118:119], v[88:89], off
	s_waitcnt vmcnt(15)
	v_lshlrev_b32_e32 v81, 16, v4
	v_and_b32_e32 v82, 0xffff0000, v4
	v_lshlrev_b32_e32 v83, 16, v5
	v_and_b32_e32 v84, 0xffff0000, v5
	v_mul_f32_e32 v81, v80, v81
	v_mul_f32_e32 v82, v80, v82
	v_mul_f32_e32 v83, v80, v83
	v_mul_f32_e32 v84, v80, v84
	v_mul_f32_e32 v81, v81, v124
	v_mul_f32_e32 v82, v82, v125
	v_mul_f32_e32 v83, v83, v126
	v_mul_f32_e32 v84, v84, v127
	v_cvt_pk_bf16_f32 v90, v81, v82
	v_cvt_pk_bf16_f32 v91, v83, v84
	global_store_dwordx2 v[118:119], v[90:91], off offset:32
	s_waitcnt vmcnt(15)
	v_lshlrev_b32_e32 v81, 16, v6
	v_and_b32_e32 v82, 0xffff0000, v6
	v_lshlrev_b32_e32 v83, 16, v7
	v_and_b32_e32 v84, 0xffff0000, v7
	v_mul_f32_e32 v81, v80, v81
	v_mul_f32_e32 v82, v80, v82
	v_mul_f32_e32 v83, v80, v83
	v_mul_f32_e32 v84, v80, v84
	v_mul_f32_e32 v81, v81, v128
	v_mul_f32_e32 v82, v82, v129
	v_mul_f32_e32 v83, v83, v130
	v_mul_f32_e32 v84, v84, v131
	v_cvt_pk_bf16_f32 v92, v81, v82
	v_cvt_pk_bf16_f32 v93, v83, v84
	global_store_dwordx2 v[118:119], v[92:93], off offset:64
	s_waitcnt vmcnt(15)
; __device__ __forceinline__ unsigned pk_bf16(float lo, float hi) { unsigned r; asm("v_cvt_pk_bf16_f32 %0, %1, %2" : "=v"(r) : "v"(lo), "v"(hi)); return r; }
; __device__ __forceinline__ float bf_lo(unsigned u) { return __uint_as_float(u << 16); }
; __device__ __forceinline__ float bf_hi(unsigned u) { return __uint_as_float(u & 0xffff0000u); }
; __device__ __forceinline__ void p4_ssd(Ctx& X, int unit) {
;     ...
;     for (int i = 0; i < 32; ++i) tv[i] = *(const u32x2*)(op + (size_t)(i >> 2) * PANE_A + 16 * (i & 3));
; #pragma unroll
;     for (int i = 0; i < 32; ++i) { const f32x4 wv = *(const f32x4*)(nw + 16 * i); const u32x2 t = tv[i];
;         u32x2 o; o.x = pk_bf16(bf_lo(t.x) * rstd * wv.x, bf_hi(t.x) * rstd * wv.y); o.y = pk_bf16(bf_lo(t.y) * rstd * wv.z, bf_hi(t.y) * rstd * wv.w);
;         *(u32x2*)(op + (size_t)(i >> 2) * PANE_A + 16 * (i & 3)) = o; }
	v_lshlrev_b32_e32 v81, 16, v8
	v_and_b32_e32 v82, 0xffff0000, v8
	v_lshlrev_b32_e32 v83, 16, v9
	v_and_b32_e32 v84, 0xffff0000, v9
	v_mul_f32_e32 v81, v80, v81
	v_mul_f32_e32 v82, v80, v82
	v_mul_f32_e32 v83, v80, v83
	v_mul_f32_e32 v84, v80, v84
	v_mul_f32_e32 v81, v81, v132
	v_mul_f32_e32 v82, v82, v133
	v_mul_f32_e32 v83, v83, v134
	v_mul_f32_e32 v84, v84, v135
	v_cvt_pk_bf16_f32 v94, v81, v82
	v_cvt_pk_bf16_f32 v95, v83, v84
	global_store_dwordx2 v[118:119], v[94:95], off offset:96
	s_waitcnt vmcnt(15)
	v_lshlrev_b32_e32 v81, 16, v10
	v_and_b32_e32 v82, 0xffff0000, v10
	v_lshlrev_b32_e32 v83, 16, v11
	v_and_b32_e32 v84, 0xffff0000, v11
	v_mul_f32_e32 v81, v80, v81
	v_mul_f32_e32 v82, v80, v82
	v_mul_f32_e32 v83, v80, v83
	v_mul_f32_e32 v84, v80, v84
	v_mul_f32_e32 v81, v81, v136
	v_mul_f32_e32 v82, v82, v137
	v_mul_f32_e32 v83, v83, v138
	v_mul_f32_e32 v84, v84, v139
	v_cvt_pk_bf16_f32 v88, v81, v82
	v_cvt_pk_bf16_f32 v89, v83, v84
	global_store_dwordx2 v[66:67], v[88:89], off
	s_waitcnt vmcnt(15)
	v_lshlrev_b32_e32 v81, 16, v12
	v_and_b32_e32 v82, 0xffff0000, v12
	v_lshlrev_b32_e32 v83, 16, v13
	v_and_b32_e32 v84, 0xffff0000, v13
	v_mul_f32_e32 v81, v80, v81
	v_mul_f32_e32 v82, v80, v82
	v_mul_f32_e32 v83, v80, v83
	v_mul_f32_e32 v84, v80, v84
	v_mul_f32_e32 v81, v81, v140
	v_mul_f32_e32 v82, v82, v141
	v_mul_f32_e32 v83, v83, v142
	v_mul_f32_e32 v84, v84, v143
	v_cvt_pk_bf16_f32 v90, v81, v82
	v_cvt_pk_bf16_f32 v91, v83, v84
	global_store_dwordx2 v[66:67], v[90:91], off offset:32
	s_waitcnt vmcnt(15)
	v_lshlrev_b32_e32 v81, 16, v14
	v_and_b32_e32 v82, 0xffff0000, v14
	v_lshlrev_b32_e32 v83, 16, v15
	v_and_b32_e32 v84, 0xffff0000, v15
	v_mul_f32_e32 v81, v80, v81
	v_mul_f32_e32 v82, v80, v82
	v_mul_f32_e32 v83, v80, v83
	v_mul_f32_e32 v84, v80, v84
	v_mul_f32_e32 v81, v81, v144
	v_mul_f32_e32 v82, v82, v145
	v_mul_f32_e32 v83, v83, v146
	v_mul_f32_e32 v84, v84, v147
	v_cvt_pk_bf16_f32 v92, v81, v82
	v_cvt_pk_bf16_f32 v93, v83, v84
	global_store_dwordx2 v[66:67], v[92:93], off offset:64
	s_waitcnt vmcnt(15)
	v_lshlrev_b32_e32 v81, 16, v16
	v_and_b32_e32 v82, 0xffff0000, v16
	v_lshlrev_b32_e32 v83, 16, v17
	v_and_b32_e32 v84, 0xffff0000, v17
	v_mul_f32_e32 v81, v80, v81
	v_mul_f32_e32 v82, v80, v82
	v_mul_f32_e32 v83, v80, v83
	v_mul_f32_e32 v84, v80, v84
	v_mul_f32_e32 v81, v81, v148
	v_mul_f32_e32 v82, v82, v149
	v_mul_f32_e32 v83, v83, v150
	v_mul_f32_e32 v84, v84, v151
	v_cvt_pk_bf16_f32 v94, v81, v82
	v_cvt_pk_bf16_f32 v95, v83, v84
	global_store_dwordx2 v[66:67], v[94:95], off offset:96
	s_waitcnt vmcnt(15)
	v_lshlrev_b32_e32 v81, 16, v18
	v_and_b32_e32 v82, 0xffff0000, v18
	v_lshlrev_b32_e32 v83, 16, v19
	v_and_b32_e32 v84, 0xffff0000, v19
	v_mul_f32_e32 v81, v80, v81
	v_mul_f32_e32 v82, v80, v82
	v_mul_f32_e32 v83, v80, v83
	v_mul_f32_e32 v84, v80, v84
	v_mul_f32_e32 v81, v81, v152
	v_mul_f32_e32 v82, v82, v153
	v_mul_f32_e32 v83, v83, v154
	v_mul_f32_e32 v84, v84, v155
	v_cvt_pk_bf16_f32 v88, v81, v82
	v_cvt_pk_bf16_f32 v89, v83, v84
	global_store_dwordx2 v[68:69], v[88:89], off
	s_waitcnt vmcnt(15)
	v_lshlrev_b32_e32 v81, 16, v20
	v_and_b32_e32 v82, 0xffff0000, v20
	v_lshlrev_b32_e32 v83, 16, v21
	v_and_b32_e32 v84, 0xffff0000, v21
	v_mul_f32_e32 v81, v80, v81
	v_mul_f32_e32 v82, v80, v82
	v_mul_f32_e32 v83, v80, v83
	v_mul_f32_e32 v84, v80, v84
	v_mul_f32_e32 v81, v81, v224
	v_mul_f32_e32 v82, v82, v225
	v_mul_f32_e32 v83, v83, v226
	v_mul_f32_e32 v84, v84, v227
	v_cvt_pk_bf16_f32 v90, v81, v82
	v_cvt_pk_bf16_f32 v91, v83, v84
	global_store_dwordx2 v[68:69], v[90:91], off offset:32
	s_waitcnt vmcnt(15)
	v_lshlrev_b32_e32 v81, 16, v22
	v_and_b32_e32 v82, 0xffff0000, v22
	v_lshlrev_b32_e32 v83, 16, v23
	v_and_b32_e32 v84, 0xffff0000, v23
	v_mul_f32_e32 v81, v80, v81
	v_mul_f32_e32 v82, v80, v82
	v_mul_f32_e32 v83, v80, v83
	v_mul_f32_e32 v84, v80, v84
	v_mul_f32_e32 v81, v81, v228
	v_mul_f32_e32 v82, v82, v229
	v_mul_f32_e32 v83, v83, v230
	v_mul_f32_e32 v84, v84, v231
	v_cvt_pk_bf16_f32 v92, v81, v82
	v_cvt_pk_bf16_f32 v93, v83, v84
	global_store_dwordx2 v[68:69], v[92:93], off offset:64
	s_waitcnt vmcnt(15)
	v_lshlrev_b32_e32 v81, 16, v24
	v_and_b32_e32 v82, 0xffff0000, v24
	v_lshlrev_b32_e32 v83, 16, v25
	v_and_b32_e32 v84, 0xffff0000, v25
	v_mul_f32_e32 v81, v80, v81
	v_mul_f32_e32 v82, v80, v82
	v_mul_f32_e32 v83, v80, v83
	v_mul_f32_e32 v84, v80, v84
	v_mul_f32_e32 v81, v81, v232
	v_mul_f32_e32 v82, v82, v233
	v_mul_f32_e32 v83, v83, v234
	v_mul_f32_e32 v84, v84, v235
	v_cvt_pk_bf16_f32 v94, v81, v82
	v_cvt_pk_bf16_f32 v95, v83, v84
	global_store_dwordx2 v[68:69], v[94:95], off offset:96
	s_waitcnt vmcnt(15)
	v_lshlrev_b32_e32 v81, 16, v26
	v_and_b32_e32 v82, 0xffff0000, v26
	v_lshlrev_b32_e32 v83, 16, v27
	v_and_b32_e32 v84, 0xffff0000, v27
	v_mul_f32_e32 v81, v80, v81
	v_mul_f32_e32 v82, v80, v82
	v_mul_f32_e32 v83, v80, v83
	v_mul_f32_e32 v84, v80, v84
	v_mul_f32_e32 v81, v81, v236
	v_mul_f32_e32 v82, v82, v237
	v_mul_f32_e32 v83, v83, v238
	v_mul_f32_e32 v84, v84, v239
	v_cvt_pk_bf16_f32 v88, v81, v82
	v_cvt_pk_bf16_f32 v89, v83, v84
	global_store_dwordx2 v[70:71], v[88:89], off
	s_waitcnt vmcnt(15)
	v_lshlrev_b32_e32 v81, 16, v28
	v_and_b32_e32 v82, 0xffff0000, v28
	v_lshlrev_b32_e32 v83, 16, v29
	v_and_b32_e32 v84, 0xffff0000, v29
	v_mul_f32_e32 v81, v80, v81
	v_mul_f32_e32 v82, v80, v82
	v_mul_f32_e32 v83, v80, v83
	v_mul_f32_e32 v84, v80, v84
	v_mul_f32_e32 v81, v81, v240
	v_mul_f32_e32 v82, v82, v241
	v_mul_f32_e32 v83, v83, v242
	v_mul_f32_e32 v84, v84, v243
	v_cvt_pk_bf16_f32 v90, v81, v82
	v_cvt_pk_bf16_f32 v91, v83, v84
	global_store_dwordx2 v[70:71], v[90:91], off offset:32
	s_waitcnt vmcnt(15)
; __device__ __forceinline__ unsigned pk_bf16(float lo, float hi) { unsigned r; asm("v_cvt_pk_bf16_f32 %0, %1, %2" : "=v"(r) : "v"(lo), "v"(hi)); return r; }
; __device__ __forceinline__ float bf_lo(unsigned u) { return __uint_as_float(u << 16); }
; __device__ __forceinline__ float bf_hi(unsigned u) { return __uint_as_float(u & 0xffff0000u); }
; __device__ __forceinline__ void p4_ssd(Ctx& X, int unit) {
;     ...
;     for (int i = 0; i < 32; ++i) tv[i] = *(const u32x2*)(op + (size_t)(i >> 2) * PANE_A + 16 * (i & 3));
; #pragma unroll
;     for (int i = 0; i < 32; ++i) { const f32x4 wv = *(const f32x4*)(nw + 16 * i); const u32x2 t = tv[i];
;         u32x2 o; o.x = pk_bf16(bf_lo(t.x) * rstd * wv.x, bf_hi(t.x) * rstd * wv.y); o.y = pk_bf16(bf_lo(t.y) * rstd * wv.z, bf_hi(t.y) * rstd * wv.w);
;         *(u32x2*)(op + (size_t)(i >> 2) * PANE_A + 16 * (i & 3)) = o; }
	v_lshlrev_b32_e32 v81, 16, v30
	v_and_b32_e32 v82, 0xffff0000, v30
	v_lshlrev_b32_e32 v83, 16, v31
	v_and_b32_e32 v84, 0xffff0000, v31
	v_mul_f32_e32 v81, v80, v81
	v_mul_f32_e32 v82, v80, v82
	v_mul_f32_e32 v83, v80, v83
	v_mul_f32_e32 v84, v80, v84
	v_mul_f32_e32 v81, v81, v244
	v_mul_f32_e32 v82, v82, v245
	v_mul_f32_e32 v83, v83, v246
	v_mul_f32_e32 v84, v84, v247
	v_cvt_pk_bf16_f32 v92, v81, v82
	v_cvt_pk_bf16_f32 v93, v83, v84
	global_store_dwordx2 v[70:71], v[92:93], off offset:64
	s_waitcnt vmcnt(15)
	v_lshlrev_b32_e32 v81, 16, v32
	v_and_b32_e32 v82, 0xffff0000, v32
	v_lshlrev_b32_e32 v83, 16, v33
	v_and_b32_e32 v84, 0xffff0000, v33
	v_mul_f32_e32 v81, v80, v81
	v_mul_f32_e32 v82, v80, v82
	v_mul_f32_e32 v83, v80, v83
	v_mul_f32_e32 v84, v80, v84
	v_mul_f32_e32 v81, v81, v214
	v_mul_f32_e32 v82, v82, v215
	v_mul_f32_e32 v83, v83, v216
	v_mul_f32_e32 v84, v84, v217
	v_cvt_pk_bf16_f32 v94, v81, v82
	v_cvt_pk_bf16_f32 v95, v83, v84
	global_store_dwordx2 v[70:71], v[94:95], off offset:96
	global_load_dwordx4 v[120:123], v87, s[6:7] offset:1024
	global_load_dwordx4 v[124:127], v87, s[6:7] offset:1088
	global_load_dwordx4 v[128:131], v87, s[6:7] offset:1152
	global_load_dwordx4 v[132:135], v87, s[6:7] offset:1216
	global_load_dwordx4 v[136:139], v87, s[6:7] offset:1280
	global_load_dwordx4 v[140:143], v87, s[6:7] offset:1344
	global_load_dwordx4 v[144:147], v87, s[6:7] offset:1408
	global_load_dwordx4 v[148:151], v87, s[6:7] offset:1472
	global_load_dwordx4 v[152:155], v87, s[6:7] offset:1536
	global_load_dwordx4 v[224:227], v87, s[6:7] offset:1600
	global_load_dwordx4 v[228:231], v87, s[6:7] offset:1664
	global_load_dwordx4 v[232:235], v87, s[6:7] offset:1728
	global_load_dwordx4 v[236:239], v87, s[6:7] offset:1792
	global_load_dwordx4 v[240:243], v87, s[6:7] offset:1856
	global_load_dwordx4 v[244:247], v87, s[6:7] offset:1920
	global_load_dwordx4 v[214:217], v87, s[6:7] offset:1984
	s_waitcnt vmcnt(15)
	v_lshlrev_b32_e32 v81, 16, v34
	v_and_b32_e32 v82, 0xffff0000, v34
	v_lshlrev_b32_e32 v83, 16, v35
	v_and_b32_e32 v84, 0xffff0000, v35
	v_mul_f32_e32 v81, v80, v81
	v_mul_f32_e32 v82, v80, v82
	v_mul_f32_e32 v83, v80, v83
	v_mul_f32_e32 v84, v80, v84
	v_mul_f32_e32 v81, v81, v120
	v_mul_f32_e32 v82, v82, v121
	v_mul_f32_e32 v83, v83, v122
	v_mul_f32_e32 v84, v84, v123
	v_cvt_pk_bf16_f32 v88, v81, v82
	v_cvt_pk_bf16_f32 v89, v83, v84
	global_store_dwordx2 v[72:73], v[88:89], off
	s_waitcnt vmcnt(15)
	v_lshlrev_b32_e32 v81, 16, v36
	v_and_b32_e32 v82, 0xffff0000, v36
	v_lshlrev_b32_e32 v83, 16, v37
	v_and_b32_e32 v84, 0xffff0000, v37
	v_mul_f32_e32 v81, v80, v81
	v_mul_f32_e32 v82, v80, v82
	v_mul_f32_e32 v83, v80, v83
	v_mul_f32_e32 v84, v80, v84
	v_mul_f32_e32 v81, v81, v124
	v_mul_f32_e32 v82, v82, v125
	v_mul_f32_e32 v83, v83, v126
	v_mul_f32_e32 v84, v84, v127
	v_cvt_pk_bf16_f32 v90, v81, v82
	v_cvt_pk_bf16_f32 v91, v83, v84
	global_store_dwordx2 v[72:73], v[90:91], off offset:32
	s_waitcnt vmcnt(15)
	v_lshlrev_b32_e32 v81, 16, v38
	v_and_b32_e32 v82, 0xffff0000, v38
	v_lshlrev_b32_e32 v83, 16, v39
	v_and_b32_e32 v84, 0xffff0000, v39
	v_mul_f32_e32 v81, v80, v81
	v_mul_f32_e32 v82, v80, v82
	v_mul_f32_e32 v83, v80, v83
	v_mul_f32_e32 v84, v80, v84
	v_mul_f32_e32 v81, v81, v128
	v_mul_f32_e32 v82, v82, v129
	v_mul_f32_e32 v83, v83, v130
	v_mul_f32_e32 v84, v84, v131
	v_cvt_pk_bf16_f32 v92, v81, v82
	v_cvt_pk_bf16_f32 v93, v83, v84
	global_store_dwordx2 v[72:73], v[92:93], off offset:64
	s_waitcnt vmcnt(15)
	v_lshlrev_b32_e32 v81, 16, v40
	v_and_b32_e32 v82, 0xffff0000, v40
	v_lshlrev_b32_e32 v83, 16, v41
	v_and_b32_e32 v84, 0xffff0000, v41
	v_mul_f32_e32 v81, v80, v81
	v_mul_f32_e32 v82, v80, v82
	v_mul_f32_e32 v83, v80, v83
	v_mul_f32_e32 v84, v80, v84
	v_mul_f32_e32 v81, v81, v132
	v_mul_f32_e32 v82, v82, v133
	v_mul_f32_e32 v83, v83, v134
	v_mul_f32_e32 v84, v84, v135
	v_cvt_pk_bf16_f32 v94, v81, v82
	v_cvt_pk_bf16_f32 v95, v83, v84
	global_store_dwordx2 v[72:73], v[94:95], off offset:96
	s_waitcnt vmcnt(15)
	v_lshlrev_b32_e32 v81, 16, v42
	v_and_b32_e32 v82, 0xffff0000, v42
	v_lshlrev_b32_e32 v83, 16, v43
	v_and_b32_e32 v84, 0xffff0000, v43
	v_mul_f32_e32 v81, v80, v81
	v_mul_f32_e32 v82, v80, v82
	v_mul_f32_e32 v83, v80, v83
	v_mul_f32_e32 v84, v80, v84
	v_mul_f32_e32 v81, v81, v136
	v_mul_f32_e32 v82, v82, v137
	v_mul_f32_e32 v83, v83, v138
	v_mul_f32_e32 v84, v84, v139
	v_cvt_pk_bf16_f32 v88, v81, v82
	v_cvt_pk_bf16_f32 v89, v83, v84
	global_store_dwordx2 v[74:75], v[88:89], off
	s_waitcnt vmcnt(15)
	v_lshlrev_b32_e32 v81, 16, v44
	v_and_b32_e32 v82, 0xffff0000, v44
	v_lshlrev_b32_e32 v83, 16, v45
	v_and_b32_e32 v84, 0xffff0000, v45
	v_mul_f32_e32 v81, v80, v81
	v_mul_f32_e32 v82, v80, v82
	v_mul_f32_e32 v83, v80, v83
	v_mul_f32_e32 v84, v80, v84
	v_mul_f32_e32 v81, v81, v140
	v_mul_f32_e32 v82, v82, v141
	v_mul_f32_e32 v83, v83, v142
	v_mul_f32_e32 v84, v84, v143
	v_cvt_pk_bf16_f32 v90, v81, v82
	v_cvt_pk_bf16_f32 v91, v83, v84
	global_store_dwordx2 v[74:75], v[90:91], off offset:32
	s_waitcnt vmcnt(15)
; __device__ __forceinline__ unsigned pk_bf16(float lo, float hi) { unsigned r; asm("v_cvt_pk_bf16_f32 %0, %1, %2" : "=v"(r) : "v"(lo), "v"(hi)); return r; }
; __device__ __forceinline__ float bf_lo(unsigned u) { return __uint_as_float(u << 16); }
; __device__ __forceinline__ float bf_hi(unsigned u) { return __uint_as_float(u & 0xffff0000u); }
; #define P4S(X,u) p4_ssd(X,u)
; __device__ __forceinline__ void p4_ssd(Ctx& X, int unit) {
;     ...
;     for (int i = 0; i < 32; ++i) tv[i] = *(const u32x2*)(op + (size_t)(i >> 2) * PANE_A + 16 * (i & 3));
; #pragma unroll
;     for (int i = 0; i < 32; ++i) { const f32x4 wv = *(const f32x4*)(nw + 16 * i); const u32x2 t = tv[i];
;         u32x2 o; o.x = pk_bf16(bf_lo(t.x) * rstd * wv.x, bf_hi(t.x) * rstd * wv.y); o.y = pk_bf16(bf_lo(t.y) * rstd * wv.z, bf_hi(t.y) * rstd * wv.w);
;         *(u32x2*)(op + (size_t)(i >> 2) * PANE_A + 16 * (i & 3)) = o; }
;     __syncthreads();
; __global__ void __launch_bounds__(NTHR, 2) fwd(Args args) {
;     ...
;         for (int u = X.bid; u < 128; u += X.G) { P4S(X, u); }
	v_lshlrev_b32_e32 v81, 16, v46
	v_and_b32_e32 v82, 0xffff0000, v46
	v_lshlrev_b32_e32 v83, 16, v47
	v_and_b32_e32 v84, 0xffff0000, v47
	v_mul_f32_e32 v81, v80, v81
	v_mul_f32_e32 v82, v80, v82
	v_mul_f32_e32 v83, v80, v83
	v_mul_f32_e32 v84, v80, v84
	v_mul_f32_e32 v81, v81, v144
	v_mul_f32_e32 v82, v82, v145
	v_mul_f32_e32 v83, v83, v146
	v_mul_f32_e32 v84, v84, v147
	v_cvt_pk_bf16_f32 v92, v81, v82
	v_cvt_pk_bf16_f32 v93, v83, v84
	global_store_dwordx2 v[74:75], v[92:93], off offset:64
	s_waitcnt vmcnt(15)
	v_lshlrev_b32_e32 v81, 16, v48
	v_and_b32_e32 v82, 0xffff0000, v48
	v_lshlrev_b32_e32 v83, 16, v49
	v_and_b32_e32 v84, 0xffff0000, v49
	v_mul_f32_e32 v81, v80, v81
	v_mul_f32_e32 v82, v80, v82
	v_mul_f32_e32 v83, v80, v83
	v_mul_f32_e32 v84, v80, v84
	v_mul_f32_e32 v81, v81, v148
	v_mul_f32_e32 v82, v82, v149
	v_mul_f32_e32 v83, v83, v150
	v_mul_f32_e32 v84, v84, v151
	v_cvt_pk_bf16_f32 v94, v81, v82
	v_cvt_pk_bf16_f32 v95, v83, v84
	global_store_dwordx2 v[74:75], v[94:95], off offset:96
	s_waitcnt vmcnt(15)
	v_lshlrev_b32_e32 v81, 16, v50
	v_and_b32_e32 v82, 0xffff0000, v50
	v_lshlrev_b32_e32 v83, 16, v51
	v_and_b32_e32 v84, 0xffff0000, v51
	v_mul_f32_e32 v81, v80, v81
	v_mul_f32_e32 v82, v80, v82
	v_mul_f32_e32 v83, v80, v83
	v_mul_f32_e32 v84, v80, v84
	v_mul_f32_e32 v81, v81, v152
	v_mul_f32_e32 v82, v82, v153
	v_mul_f32_e32 v83, v83, v154
	v_mul_f32_e32 v84, v84, v155
	v_cvt_pk_bf16_f32 v88, v81, v82
	v_cvt_pk_bf16_f32 v89, v83, v84
	global_store_dwordx2 v[76:77], v[88:89], off
	s_waitcnt vmcnt(15)
	v_lshlrev_b32_e32 v81, 16, v52
	v_and_b32_e32 v82, 0xffff0000, v52
	v_lshlrev_b32_e32 v83, 16, v53
	v_and_b32_e32 v84, 0xffff0000, v53
	v_mul_f32_e32 v81, v80, v81
	v_mul_f32_e32 v82, v80, v82
	v_mul_f32_e32 v83, v80, v83
	v_mul_f32_e32 v84, v80, v84
	v_mul_f32_e32 v81, v81, v224
	v_mul_f32_e32 v82, v82, v225
	v_mul_f32_e32 v83, v83, v226
	v_mul_f32_e32 v84, v84, v227
	v_cvt_pk_bf16_f32 v90, v81, v82
	v_cvt_pk_bf16_f32 v91, v83, v84
	global_store_dwordx2 v[76:77], v[90:91], off offset:32
	s_waitcnt vmcnt(15)
	v_lshlrev_b32_e32 v81, 16, v54
	v_and_b32_e32 v82, 0xffff0000, v54
	v_lshlrev_b32_e32 v83, 16, v55
	v_and_b32_e32 v84, 0xffff0000, v55
	v_mul_f32_e32 v81, v80, v81
	v_mul_f32_e32 v82, v80, v82
	v_mul_f32_e32 v83, v80, v83
	v_mul_f32_e32 v84, v80, v84
	v_mul_f32_e32 v81, v81, v228
	v_mul_f32_e32 v82, v82, v229
	v_mul_f32_e32 v83, v83, v230
	v_mul_f32_e32 v84, v84, v231
	v_cvt_pk_bf16_f32 v92, v81, v82
	v_cvt_pk_bf16_f32 v93, v83, v84
	global_store_dwordx2 v[76:77], v[92:93], off offset:64
	s_waitcnt vmcnt(15)
	v_lshlrev_b32_e32 v81, 16, v56
	v_and_b32_e32 v82, 0xffff0000, v56
	v_lshlrev_b32_e32 v83, 16, v57
	v_and_b32_e32 v84, 0xffff0000, v57
	v_mul_f32_e32 v81, v80, v81
	v_mul_f32_e32 v82, v80, v82
	v_mul_f32_e32 v83, v80, v83
	v_mul_f32_e32 v84, v80, v84
	v_mul_f32_e32 v81, v81, v232
	v_mul_f32_e32 v82, v82, v233
	v_mul_f32_e32 v83, v83, v234
	v_mul_f32_e32 v84, v84, v235
	v_cvt_pk_bf16_f32 v94, v81, v82
	v_cvt_pk_bf16_f32 v95, v83, v84
	global_store_dwordx2 v[76:77], v[94:95], off offset:96
	s_waitcnt vmcnt(15)
	v_lshlrev_b32_e32 v81, 16, v58
	v_and_b32_e32 v82, 0xffff0000, v58
	v_lshlrev_b32_e32 v83, 16, v59
	v_and_b32_e32 v84, 0xffff0000, v59
	v_mul_f32_e32 v81, v80, v81
	v_mul_f32_e32 v82, v80, v82
	v_mul_f32_e32 v83, v80, v83
	v_mul_f32_e32 v84, v80, v84
	v_mul_f32_e32 v81, v81, v236
	v_mul_f32_e32 v82, v82, v237
	v_mul_f32_e32 v83, v83, v238
	v_mul_f32_e32 v84, v84, v239
	v_cvt_pk_bf16_f32 v88, v81, v82
	v_cvt_pk_bf16_f32 v89, v83, v84
	global_store_dwordx2 v[78:79], v[88:89], off
	s_waitcnt vmcnt(15)
	v_lshlrev_b32_e32 v81, 16, v60
	v_and_b32_e32 v82, 0xffff0000, v60
	v_lshlrev_b32_e32 v83, 16, v61
	v_and_b32_e32 v84, 0xffff0000, v61
	v_mul_f32_e32 v81, v80, v81
	v_mul_f32_e32 v82, v80, v82
	v_mul_f32_e32 v83, v80, v83
	v_mul_f32_e32 v84, v80, v84
	v_mul_f32_e32 v81, v81, v240
	v_mul_f32_e32 v82, v82, v241
	v_mul_f32_e32 v83, v83, v242
	v_mul_f32_e32 v84, v84, v243
	v_cvt_pk_bf16_f32 v90, v81, v82
	v_cvt_pk_bf16_f32 v91, v83, v84
	global_store_dwordx2 v[78:79], v[90:91], off offset:32
	s_waitcnt vmcnt(15)
	v_lshlrev_b32_e32 v81, 16, v62
	v_and_b32_e32 v82, 0xffff0000, v62
	v_lshlrev_b32_e32 v83, 16, v63
	v_and_b32_e32 v84, 0xffff0000, v63
	v_mul_f32_e32 v81, v80, v81
	v_mul_f32_e32 v82, v80, v82
	v_mul_f32_e32 v83, v80, v83
	v_mul_f32_e32 v84, v80, v84
	v_mul_f32_e32 v81, v81, v244
	v_mul_f32_e32 v82, v82, v245
	v_mul_f32_e32 v83, v83, v246
	v_mul_f32_e32 v84, v84, v247
	v_cvt_pk_bf16_f32 v92, v81, v82
	v_cvt_pk_bf16_f32 v93, v83, v84
	global_store_dwordx2 v[78:79], v[92:93], off offset:64
	s_waitcnt vmcnt(15)
	v_lshlrev_b32_e32 v81, 16, v64
	v_and_b32_e32 v82, 0xffff0000, v64
	v_lshlrev_b32_e32 v83, 16, v65
	v_and_b32_e32 v84, 0xffff0000, v65
	v_mul_f32_e32 v81, v80, v81
	v_mul_f32_e32 v82, v80, v82
	v_mul_f32_e32 v83, v80, v83
	v_mul_f32_e32 v84, v80, v84
	v_mul_f32_e32 v81, v81, v214
	v_mul_f32_e32 v82, v82, v215
	v_mul_f32_e32 v83, v83, v216
	v_mul_f32_e32 v84, v84, v217
	v_cvt_pk_bf16_f32 v94, v81, v82
	v_cvt_pk_bf16_f32 v95, v83, v84
	global_store_dwordx2 v[78:79], v[94:95], off offset:96
	s_load_dword s92, s[0:1], 0xb0
	v_readlane_b32 s6, v248, 42
	v_readlane_b32 s7, v248, 43
	s_waitcnt lgkmcnt(0)
	s_add_i32 s11, s11, s92
	s_xor_b64 s[2:3], s[2:3], s[6:7]
	s_cmpk_gt_i32 s11, 0x7f
	s_barrier
	s_cbranch_scc1 .LBB0_661

; #define LAS __attribute__((address_space(3)))
; __device__ __forceinline__ unsigned pk_bf16(float lo, float hi) { unsigned r; asm("v_cvt_pk_bf16_f32 %0, %1, %2" : "=v"(r) : "v"(lo), "v"(hi)); return r; }
; __device__ __forceinline__ f32x4 mma16(bf16x8 xrow, bf16x8 ycol, f32x4 c) { return __builtin_amdgcn_mfma_f32_16x16x32_bf16(xrow, ycol, c, 0, 0, 0); }
; __device__ __forceinline__ void p4_ssd(Ctx& X, int unit) {
;     ...
; #pragma unroll
;             for (int n = 0; n < 4; ++n) y[n] = (f32x4){0.f, 0.f, 0.f, 0.f};
; #pragma unroll
;             for (int ks = 0; ks < 4; ++ks)
; #pragma unroll
;                 for (int n = 0; n < 4; ++n) { const bf16x8 bf = *(const LAS bf16x8*)(Ph + (16 * n + fr) * 272 + (32 * ks + 8 * fq) * 2); y[n] = mma16(bf, cfr[ks], y[n]); }
;             const float al = acS[e * 128 + l], el = __expf(al);
; #pragma unroll
;             for (int n = 0; n < 4; ++n) y[n] = y[n] * el;
; #pragma unroll
;             for (int k2 = 0; k2 < 4; ++k2) if (2 * k2 <= w) { float v[8];
; #pragma unroll
;                 for (int tq = 0; tq < 2; ++tq) { const int s0 = 16 * (2 * k2 + tq) + 4 * fq; const f32x4 as = *(const LAS f32x4*)(acS + e * 128 + s0), ds = *(const LAS f32x4*)(dtS + e * 128 + s0);
; #pragma unroll
;                     for (int j = 0; j < 4; ++j) v[4 * tq + j] = (s0 + j <= l) ? cb[2 * k2 + tq][j] * ds[j] * __expf(al - as[j]) : 0.f; }
;                 u32x4 pk; pk.x = pk_bf16(v[0], v[1]); pk.y = pk_bf16(v[2], v[3]); pk.z = pk_bf16(v[4], v[5]); pk.w = pk_bf16(v[6], v[7]);
;                 const bf16x8 gf = __builtin_bit_cast(bf16x8, pk);
; #pragma unroll
;                 for (int n = 0; n < 4; ++n) { const bf16x8 bf = tr_frag(Xh + (32 * k2) * 144 + (16 * n) * 2 + trp, 16 * 144); y[n] = mma16(bf, gf, y[n]); }
.LBB0_629:
	ds_read_b128 v[228:231], v203
	ds_read_b128 v[232:235], v203 offset:64
	ds_read_b128 v[236:239], v203 offset:4352
	ds_read_b128 v[240:243], v203 offset:4416
	ds_read_b128 v[244:247], v203 offset:8704
	ds_read_b128 v[250:253], v203 offset:8768
	s_lshl_b32 s4, s92, 9
	s_add_i32 s6, s4, 0
	s_add_i32 s6, s6, 0x1c000
	s_and_b64 vcc, exec, s[82:83]
	s_waitcnt lgkmcnt(5)
	v_mfma_f32_16x16x32_bf16 v[82:85], v[228:231], v[34:37], 0
	ds_read_b128 v[228:231], v203 offset:13056
	s_waitcnt lgkmcnt(5)
	v_mfma_f32_16x16x32_bf16 v[82:85], v[232:235], v[66:69], v[82:85]
	ds_read_b128 v[232:235], v203 offset:13120
	s_waitcnt lgkmcnt(5)
	v_mfma_f32_16x16x32_bf16 v[86:89], v[236:239], v[34:37], 0
	ds_read_b128 v[236:239], v203 offset:128
	s_waitcnt lgkmcnt(5)
	v_mfma_f32_16x16x32_bf16 v[86:89], v[240:243], v[66:69], v[86:89]
	ds_read_b128 v[240:243], v203 offset:4480
	s_waitcnt lgkmcnt(5)
	v_mfma_f32_16x16x32_bf16 v[160:163], v[244:247], v[34:37], 0
	ds_read_b128 v[244:247], v203 offset:8832
	s_waitcnt lgkmcnt(5)
	v_mfma_f32_16x16x32_bf16 v[160:163], v[250:253], v[66:69], v[160:163]
	ds_read_b128 v[250:253], v203 offset:13184
	s_waitcnt lgkmcnt(5)
	v_mfma_f32_16x16x32_bf16 v[208:211], v[228:231], v[34:37], 0
	ds_read_b128 v[228:231], v203 offset:192
	s_waitcnt lgkmcnt(5)
	v_mfma_f32_16x16x32_bf16 v[208:211], v[232:235], v[66:69], v[208:211]
	ds_read_b128 v[232:235], v203 offset:4544
	s_waitcnt lgkmcnt(5)
	v_mfma_f32_16x16x32_bf16 v[82:85], v[236:239], v[70:73], v[82:85]
	ds_read_b128 v[236:239], v203 offset:8896
	s_waitcnt lgkmcnt(5)
	v_mfma_f32_16x16x32_bf16 v[86:89], v[240:243], v[70:73], v[86:89]
	ds_read_b128 v[240:243], v203 offset:13248
	s_waitcnt lgkmcnt(5)
	v_mfma_f32_16x16x32_bf16 v[160:163], v[244:247], v[70:73], v[160:163]
	s_waitcnt lgkmcnt(4)
	v_mfma_f32_16x16x32_bf16 v[208:211], v[250:253], v[70:73], v[208:211]
	s_waitcnt lgkmcnt(3)
	v_mfma_f32_16x16x32_bf16 v[82:85], v[228:231], v[74:77], v[82:85]
	s_waitcnt lgkmcnt(2)
	v_mfma_f32_16x16x32_bf16 v[86:89], v[232:235], v[74:77], v[86:89]
	s_waitcnt lgkmcnt(1)
	v_mfma_f32_16x16x32_bf16 v[160:163], v[236:239], v[74:77], v[160:163]
	s_waitcnt lgkmcnt(0)
	v_mfma_f32_16x16x32_bf16 v[208:211], v[240:243], v[74:77], v[208:211]
	v_lshl_add_u32 v90, v99, 2, s6
	ds_read_b32 v117, v90
	s_waitcnt lgkmcnt(0)
	v_mul_f32_e32 v90, 0x3fb8aa3b, v117
	v_exp_f32_e32 v212, v90
	s_nop 0
	v_pk_mul_f32 v[90:91], v[86:87], v[212:213] op_sel_hi:[1,0]
	v_pk_mul_f32 v[86:87], v[160:161], v[212:213] op_sel_hi:[1,0]
	v_lshl_add_u32 v160, v98, 2, s6
	v_pk_mul_f32 v[96:97], v[84:85], v[212:213] op_sel_hi:[1,0]
	v_pk_mul_f32 v[94:95], v[82:83], v[212:213] op_sel_hi:[1,0]
	v_pk_mul_f32 v[84:85], v[210:211], v[212:213] op_sel_hi:[1,0]
	v_pk_mul_f32 v[82:83], v[208:209], v[212:213] op_sel_hi:[1,0]
	ds_read_b128 v[208:211], v160
	v_add_u32_e32 v161, s4, v184
	v_pk_mul_f32 v[92:93], v[88:89], v[212:213] op_sel_hi:[1,0]
	v_pk_mul_f32 v[88:89], v[162:163], v[212:213] op_sel_hi:[1,0]
	ds_read_b128 v[212:215], v161
	s_waitcnt lgkmcnt(1)
	v_sub_f32_e32 v163, v117, v208
	v_mul_f32_e32 v163, 0x3fb8aa3b, v163
	v_sub_f32_e32 v208, v117, v209
	v_exp_f32_e32 v163, v163
	v_mul_f32_e32 v208, 0x3fb8aa3b, v208
	v_sub_f32_e32 v209, v117, v210
	v_exp_f32_e32 v208, v208
	v_mul_f32_e32 v209, 0x3fb8aa3b, v209
	v_exp_f32_e32 v209, v209
	s_waitcnt lgkmcnt(0)
	v_mul_f32_e32 v162, v78, v212
	v_mul_f32_e32 v162, v162, v163
	v_mul_f32_e32 v163, v79, v213
	v_mul_f32_e32 v163, v163, v208
	v_mul_f32_e32 v208, v80, v214
	v_mul_f32_e32 v208, v208, v209
	v_sub_f32_e32 v209, v117, v211
	v_mul_f32_e32 v209, 0x3fb8aa3b, v209
	v_exp_f32_e32 v209, v209
	v_cndmask_b32_e64 v216, v208, 0, s[20:21]
	v_mul_f32_e32 v208, v81, v215
	v_cndmask_b32_e64 v162, v162, 0, s[16:17]
	v_mul_f32_e32 v208, v208, v209
	v_cndmask_b32_e64 v217, v208, 0, s[22:23]
	ds_read_b128 v[208:211], v160 offset:64
	ds_read_b128 v[212:215], v161 offset:64
	v_cndmask_b32_e64 v163, 0, v163, s[18:19]
	s_waitcnt lgkmcnt(1)
	v_sub_f32_e32 v208, v117, v208
	v_mul_f32_e32 v208, 0x3fb8aa3b, v208
	v_exp_f32_e32 v208, v208
	v_sub_f32_e32 v209, v117, v209
	v_mul_f32_e32 v209, 0x3fb8aa3b, v209
	v_exp_f32_e32 v209, v209
	s_waitcnt lgkmcnt(0)
	v_mul_f32_e32 v212, v38, v212
	v_mul_f32_e32 v208, v212, v208
	v_cndmask_b32_e64 v212, v208, 0, s[24:25]
	v_mul_f32_e32 v208, v39, v213
	v_mul_f32_e32 v208, v208, v209
	v_sub_f32_e32 v209, v117, v210
	v_mul_f32_e32 v209, 0x3fb8aa3b, v209
	v_exp_f32_e32 v209, v209
	v_cndmask_b32_e64 v213, 0, v208, s[26:27]
	v_mul_f32_e32 v208, v40, v214
	v_cvt_pk_bf16_f32 v210, v212, v213
	v_mul_f32_e32 v208, v208, v209
	v_sub_f32_e32 v209, v117, v211
	v_mul_f32_e32 v209, 0x3fb8aa3b, v209
	v_exp_f32_e32 v209, v209
	v_cndmask_b32_e64 v214, v208, 0, s[28:29]
	v_mul_f32_e32 v208, v41, v215
	v_mul_f32_e32 v208, v208, v209
	v_cndmask_b32_e64 v211, v208, 0, s[30:31]
	v_cvt_pk_bf16_f32 v209, v216, v217
	v_cvt_pk_bf16_f32 v211, v214, v211
	ds_read_b64_tr_b16 v[214:215], v180 offset:37120
	ds_read_b64_tr_b16 v[212:213], v180 offset:34816
	ds_read_b64_tr_b16 v[216:217], v180 offset:34848
	v_cvt_pk_bf16_f32 v208, v162, v163
	ds_read_b64_tr_b16 v[218:219], v180 offset:37152
	s_waitcnt lgkmcnt(2)
	v_mfma_f32_16x16x32_bf16 v[94:97], v[212:215], v[208:211], v[94:97]
	ds_read_b64_tr_b16 v[212:213], v180 offset:34880
	ds_read_b64_tr_b16 v[214:215], v180 offset:37184
	s_waitcnt lgkmcnt(0)
	v_mfma_f32_16x16x32_bf16 v[86:89], v[212:215], v[208:211], v[86:89]
	ds_read_b64_tr_b16 v[212:213], v180 offset:34912
	ds_read_b64_tr_b16 v[214:215], v180 offset:37216
	v_mfma_f32_16x16x32_bf16 v[90:93], v[216:219], v[208:211], v[90:93]
	s_waitcnt lgkmcnt(0)
	v_mfma_f32_16x16x32_bf16 v[82:85], v[212:215], v[208:211], v[82:85]
	s_cbranch_vccz .LBB0_639
	s_and_b64 vcc, exec, s[84:85]
	s_cbranch_vccz .LBB0_640
